# speedup vs baseline: 1.0039x; 1.0039x over previous
.LBB1_103:
	v_cmp_eq_u32_e64 s[0:1], 0, v194
	v_add_f32_dpp v201, v201, v201 quad_perm:[1,0,3,2] row_mask:0xf bank_mask:0xf bound_ctrl:1
	s_nop 1
	v_add_f32_dpp v201, v201, v201 quad_perm:[2,3,0,1] row_mask:0xf bank_mask:0xf bound_ctrl:1
	s_nop 1
	v_add_f32_dpp v201, v201, v201 row_half_mirror row_mask:0xf bank_mask:0xf bound_ctrl:1
	s_nop 1
	v_add_f32_dpp v201, v201, v201 row_mirror row_mask:0xf bank_mask:0xf bound_ctrl:1
	s_nop 1
	v_add_f32_dpp v201, v201, v201 row_bcast:15 row_mask:0xa bank_mask:0xf bound_ctrl:1
	s_nop 1
	v_add_f32_dpp v201, v201, v201 row_bcast:31 row_mask:0xc bank_mask:0xf bound_ctrl:1
	s_nop 1
	v_readlane_b32 s5, v201, 63
	s_and_saveexec_b64 s[2:3], s[0:1]
	s_cbranch_execz .LBB1_105
	s_lshl_b32 s4, s52, 2
	v_mov_b32_e32 v8, s5
	v_mov_b32_e32 v9, s4
	ds_write_b32 v9, v8 offset:37632

.LBB1_114:
	s_or_b64 exec, exec, s[0:1]
	s_waitcnt vmcnt(0)
	v_add_f32_dpp v8, v8, v8 quad_perm:[1,0,3,2] row_mask:0xf bank_mask:0xf bound_ctrl:1
	v_add_f32_dpp v9, v9, v9 quad_perm:[1,0,3,2] row_mask:0xf bank_mask:0xf bound_ctrl:1
	s_nop 0
	v_add_f32_dpp v8, v8, v8 quad_perm:[2,3,0,1] row_mask:0xf bank_mask:0xf bound_ctrl:1
	v_add_f32_dpp v9, v9, v9 quad_perm:[2,3,0,1] row_mask:0xf bank_mask:0xf bound_ctrl:1
	s_nop 0
	v_add_f32_dpp v8, v8, v8 row_half_mirror row_mask:0xf bank_mask:0xf bound_ctrl:1
	v_add_f32_dpp v9, v9, v9 row_half_mirror row_mask:0xf bank_mask:0xf bound_ctrl:1
	s_nop 0
	v_add_f32_dpp v8, v8, v8 row_mirror row_mask:0xf bank_mask:0xf bound_ctrl:1
	v_add_f32_dpp v9, v9, v9 row_mirror row_mask:0xf bank_mask:0xf bound_ctrl:1
	s_nop 0
	v_add_f32_dpp v8, v8, v8 row_bcast:15 row_mask:0xa bank_mask:0xf bound_ctrl:1
	v_add_f32_dpp v9, v9, v9 row_bcast:15 row_mask:0xa bank_mask:0xf bound_ctrl:1
	s_nop 0
	v_add_f32_dpp v8, v8, v8 row_bcast:31 row_mask:0xc bank_mask:0xf bound_ctrl:1
	v_add_f32_dpp v9, v9, v9 row_bcast:31 row_mask:0xc bank_mask:0xf bound_ctrl:1
	s_nop 0
	v_and_b32_e32 v6, 0x13f, v0
	v_cmp_eq_u32_e32 vcc, 63, v6
	s_and_saveexec_b64 s[0:1], vcc
	s_cbranch_execz .LBB1_116
	v_mov_b32_e32 v3, v9
	v_mov_b32_e32 v2, v8
	v_max_f32_e32 v3, 0x358637bd, v3
	v_div_scale_f32 v4, s[2:3], v3, v3, v2
	v_rcp_f32_e32 v5, v4
	v_lshlrev_b32_e32 v1, 2, v1
	v_fma_f32 v6, -v4, v5, 1.0
	v_fmac_f32_e32 v5, v6, v5
	v_div_scale_f32 v6, vcc, v2, v3, v2
	v_mul_f32_e32 v7, v6, v5
	v_fma_f32 v8, -v4, v7, v6
	v_fmac_f32_e32 v7, v8, v5
	v_fma_f32 v4, -v4, v7, v6
	v_div_fmas_f32 v4, v4, v5, v7
	v_div_fixup_f32 v2, v4, v3, v2
	ds_write_b32 v1, v2 offset:37664
